# prologue tail loops (x->bf16, LoRA weight gather) restructured to keep 8 loads in flight per lane
# speedup vs baseline: 1.0070x; 1.0035x over previous
.LBB0_56:
	s_or_b64 exec, exec, s[10:11]
	v_lshl_add_u32 v2, s6, 9, v6
	s_mov_b32 s3, 0xf0000
	v_cmp_gt_i32_e32 vcc, s3, v2
	s_and_saveexec_b64 s[10:11], vcc
	s_cbranch_execz .LBB0_65
	s_lshl_b32 s12, s2, 9
	v_ashrrev_i32_e32 v3, 31, v2
	v_lshl_add_u64 v[4:5], v[2:3], 1, s[4:5]
	s_mov_b64 s[14:15], 0x55484800
	s_ashr_i32 s13, s12, 31
	v_lshl_add_u64 v[4:5], v[4:5], 0, s[14:15]
	s_lshl_b64 s[14:15], s[12:13], 1
	s_mov_b64 s[16:17], 0
	s_mov_b32 s3, 0x88888889
	s_movk_i32 s13, 0x5ff
	v_mov_b32_e32 v9, 0
	s_movk_i32 s22, 0x2aab
	s_mov_b32 s23, 0xeffff
	v_mov_b32_e32 v3, 0x50
	v_mov_b32_e32 v10, v2
	s_movk_i32 s66, 0x600
	s_movk_i32 s67, 0x300
	s_movk_i32 s68, 0x180
	v_mov_b32_e32 v20, 0x300
	v_mov_b32_e32 v21, 0x180
	s_load_dwordx2 s[16:17], s[8:9], 0x40
	s_load_dwordx2 s[18:19], s[8:9], 0x50
	s_load_dwordx2 s[20:21], s[8:9], 0x58
	s_mov_b32 s22, 0x88888889
	s_mov_b32 s23, 0xf0000
	s_waitcnt lgkmcnt(0)
.Llora_trip:
	s_mov_b64 s[40:41], exec
	v_and_b32_e32 v11, 0x7f, v10
	v_lshrrev_b32_e32 v12, 7, v10
	v_lshrrev_b32_e32 v13, 7, v12
	v_mul_hi_u32 v13, v13, s22
	v_lshrrev_b32_e32 v13, 3, v13
	v_mul_u32_u24_e32 v14, 0x780, v13
	v_sub_u32_e32 v14, v12, v14
	v_cmp_le_u32_e64 s[56:57], s66, v14
	v_cmp_le_u32_e64 s[58:59], s67, v14
	v_mov_b32_e32 v30, 0
	v_cmp_gt_u32_e64 s[62:63], 64, v11
	v_cndmask_b32_e64 v15, 0, v20, s[58:59]
	v_sub_u32_e32 v15, v14, v15
	v_cmp_le_u32_e64 s[60:61], s68, v15
	s_nop 1
	v_cndmask_b32_e64 v16, 0, v21, s[60:61]
	v_sub_u32_e32 v16, v15, v16
	v_cndmask_b32_e64 v17, 0, 1, s[60:61]
	v_lshl_add_u32 v17, v13, 1, v17
	v_lshl_add_u32 v17, v17, 6, v11
	v_mad_u32_u24 v17, v17, v21, v16
	v_lshl_add_u32 v18, v13, 7, v11
	v_subrev_u32_e32 v19, s66, v14
	v_mad_u32_u24 v18, v18, v21, v19
	v_cndmask_b32_e64 v26, v17, v18, s[56:57]
	v_mov_b32_e32 v22, s16
	v_mov_b32_e32 v23, s17
	v_mov_b32_e32 v24, s18
	v_mov_b32_e32 v25, s19
	v_cndmask_b32_e64 v22, v22, v24, s[58:59]
	v_cndmask_b32_e64 v23, v23, v25, s[58:59]
	v_mov_b32_e32 v24, s20
	v_mov_b32_e32 v25, s21
	v_cndmask_b32_e64 v22, v22, v24, s[56:57]
	v_cndmask_b32_e64 v23, v23, v25, s[56:57]
	v_mov_b32_e32 v27, 0
	v_lshl_add_u64 v[22:23], v[26:27], 2, v[22:23]
	s_or_b64 s[62:63], s[62:63], s[56:57]
	s_and_b64 exec, exec, s[62:63]
	global_load_dword v30, v[22:23], off
	s_mov_b64 exec, s[40:41]
	v_add_u32_e32 v10, s12, v10
	v_cmp_gt_u32_e32 vcc, s23, v10
	s_and_b64 exec, exec, vcc
	s_mov_b64 s[42:43], exec
	v_and_b32_e32 v11, 0x7f, v10
	v_lshrrev_b32_e32 v12, 7, v10
	v_lshrrev_b32_e32 v13, 7, v12
	v_mul_hi_u32 v13, v13, s22
	v_lshrrev_b32_e32 v13, 3, v13
	v_mul_u32_u24_e32 v14, 0x780, v13
	v_sub_u32_e32 v14, v12, v14
	v_cmp_le_u32_e64 s[56:57], s66, v14
	v_cmp_le_u32_e64 s[58:59], s67, v14
	v_mov_b32_e32 v31, 0
	v_cmp_gt_u32_e64 s[62:63], 64, v11
	v_cndmask_b32_e64 v15, 0, v20, s[58:59]
	v_sub_u32_e32 v15, v14, v15
	v_cmp_le_u32_e64 s[60:61], s68, v15
	s_nop 1
	v_cndmask_b32_e64 v16, 0, v21, s[60:61]
	v_sub_u32_e32 v16, v15, v16
	v_cndmask_b32_e64 v17, 0, 1, s[60:61]
	v_lshl_add_u32 v17, v13, 1, v17
	v_lshl_add_u32 v17, v17, 6, v11
	v_mad_u32_u24 v17, v17, v21, v16
	v_lshl_add_u32 v18, v13, 7, v11
	v_subrev_u32_e32 v19, s66, v14
	v_mad_u32_u24 v18, v18, v21, v19
	v_cndmask_b32_e64 v26, v17, v18, s[56:57]
	v_mov_b32_e32 v22, s16
	v_mov_b32_e32 v23, s17
	v_mov_b32_e32 v24, s18
	v_mov_b32_e32 v25, s19
	v_cndmask_b32_e64 v22, v22, v24, s[58:59]
	v_cndmask_b32_e64 v23, v23, v25, s[58:59]
	v_mov_b32_e32 v24, s20
	v_mov_b32_e32 v25, s21
	v_cndmask_b32_e64 v22, v22, v24, s[56:57]
	v_cndmask_b32_e64 v23, v23, v25, s[56:57]
	v_mov_b32_e32 v27, 0
	v_lshl_add_u64 v[22:23], v[26:27], 2, v[22:23]
	s_or_b64 s[62:63], s[62:63], s[56:57]
	s_and_b64 exec, exec, s[62:63]
	global_load_dword v31, v[22:23], off
	s_mov_b64 exec, s[42:43]
	v_add_u32_e32 v10, s12, v10
	v_cmp_gt_u32_e32 vcc, s23, v10
	s_and_b64 exec, exec, vcc
	s_mov_b64 s[44:45], exec
	v_and_b32_e32 v11, 0x7f, v10
	v_lshrrev_b32_e32 v12, 7, v10
	v_lshrrev_b32_e32 v13, 7, v12
	v_mul_hi_u32 v13, v13, s22
	v_lshrrev_b32_e32 v13, 3, v13
	v_mul_u32_u24_e32 v14, 0x780, v13
	v_sub_u32_e32 v14, v12, v14
	v_cmp_le_u32_e64 s[56:57], s66, v14
	v_cmp_le_u32_e64 s[58:59], s67, v14
	v_mov_b32_e32 v32, 0
	v_cmp_gt_u32_e64 s[62:63], 64, v11
	v_cndmask_b32_e64 v15, 0, v20, s[58:59]
	v_sub_u32_e32 v15, v14, v15
	v_cmp_le_u32_e64 s[60:61], s68, v15
	s_nop 1
	v_cndmask_b32_e64 v16, 0, v21, s[60:61]
	v_sub_u32_e32 v16, v15, v16
	v_cndmask_b32_e64 v17, 0, 1, s[60:61]
	v_lshl_add_u32 v17, v13, 1, v17
	v_lshl_add_u32 v17, v17, 6, v11
	v_mad_u32_u24 v17, v17, v21, v16
	v_lshl_add_u32 v18, v13, 7, v11
	v_subrev_u32_e32 v19, s66, v14
	v_mad_u32_u24 v18, v18, v21, v19
	v_cndmask_b32_e64 v26, v17, v18, s[56:57]
	v_mov_b32_e32 v22, s16
	v_mov_b32_e32 v23, s17
	v_mov_b32_e32 v24, s18
	v_mov_b32_e32 v25, s19
	v_cndmask_b32_e64 v22, v22, v24, s[58:59]
	v_cndmask_b32_e64 v23, v23, v25, s[58:59]
	v_mov_b32_e32 v24, s20
	v_mov_b32_e32 v25, s21
	v_cndmask_b32_e64 v22, v22, v24, s[56:57]
	v_cndmask_b32_e64 v23, v23, v25, s[56:57]
	v_mov_b32_e32 v27, 0
	v_lshl_add_u64 v[22:23], v[26:27], 2, v[22:23]
	s_or_b64 s[62:63], s[62:63], s[56:57]
	s_and_b64 exec, exec, s[62:63]
	global_load_dword v32, v[22:23], off
	s_mov_b64 exec, s[44:45]
	v_add_u32_e32 v10, s12, v10
	v_cmp_gt_u32_e32 vcc, s23, v10
	s_and_b64 exec, exec, vcc
	s_mov_b64 s[46:47], exec
	v_and_b32_e32 v11, 0x7f, v10
	v_lshrrev_b32_e32 v12, 7, v10
	v_lshrrev_b32_e32 v13, 7, v12
	v_mul_hi_u32 v13, v13, s22
	v_lshrrev_b32_e32 v13, 3, v13
	v_mul_u32_u24_e32 v14, 0x780, v13
	v_sub_u32_e32 v14, v12, v14
	v_cmp_le_u32_e64 s[56:57], s66, v14
	v_cmp_le_u32_e64 s[58:59], s67, v14
	v_mov_b32_e32 v33, 0
	v_cmp_gt_u32_e64 s[62:63], 64, v11
	v_cndmask_b32_e64 v15, 0, v20, s[58:59]
	v_sub_u32_e32 v15, v14, v15
	v_cmp_le_u32_e64 s[60:61], s68, v15
	s_nop 1
	v_cndmask_b32_e64 v16, 0, v21, s[60:61]
	v_sub_u32_e32 v16, v15, v16
	v_cndmask_b32_e64 v17, 0, 1, s[60:61]
	v_lshl_add_u32 v17, v13, 1, v17
	v_lshl_add_u32 v17, v17, 6, v11
	v_mad_u32_u24 v17, v17, v21, v16
	v_lshl_add_u32 v18, v13, 7, v11
	v_subrev_u32_e32 v19, s66, v14
	v_mad_u32_u24 v18, v18, v21, v19
	v_cndmask_b32_e64 v26, v17, v18, s[56:57]
	v_mov_b32_e32 v22, s16
	v_mov_b32_e32 v23, s17
	v_mov_b32_e32 v24, s18
	v_mov_b32_e32 v25, s19
	v_cndmask_b32_e64 v22, v22, v24, s[58:59]
	v_cndmask_b32_e64 v23, v23, v25, s[58:59]
	v_mov_b32_e32 v24, s20
	v_mov_b32_e32 v25, s21
	v_cndmask_b32_e64 v22, v22, v24, s[56:57]
	v_cndmask_b32_e64 v23, v23, v25, s[56:57]
	v_mov_b32_e32 v27, 0
	v_lshl_add_u64 v[22:23], v[26:27], 2, v[22:23]
	s_or_b64 s[62:63], s[62:63], s[56:57]
	s_and_b64 exec, exec, s[62:63]
	global_load_dword v33, v[22:23], off
	s_mov_b64 exec, s[46:47]
	v_add_u32_e32 v10, s12, v10
	v_cmp_gt_u32_e32 vcc, s23, v10
	s_and_b64 exec, exec, vcc
	s_mov_b64 s[48:49], exec
	v_and_b32_e32 v11, 0x7f, v10
	v_lshrrev_b32_e32 v12, 7, v10
	v_lshrrev_b32_e32 v13, 7, v12
	v_mul_hi_u32 v13, v13, s22
	v_lshrrev_b32_e32 v13, 3, v13
	v_mul_u32_u24_e32 v14, 0x780, v13
	v_sub_u32_e32 v14, v12, v14
	v_cmp_le_u32_e64 s[56:57], s66, v14
	v_cmp_le_u32_e64 s[58:59], s67, v14
	v_mov_b32_e32 v34, 0
	v_cmp_gt_u32_e64 s[62:63], 64, v11
	v_cndmask_b32_e64 v15, 0, v20, s[58:59]
	v_sub_u32_e32 v15, v14, v15
	v_cmp_le_u32_e64 s[60:61], s68, v15
	s_nop 1
	v_cndmask_b32_e64 v16, 0, v21, s[60:61]
	v_sub_u32_e32 v16, v15, v16
	v_cndmask_b32_e64 v17, 0, 1, s[60:61]
	v_lshl_add_u32 v17, v13, 1, v17
	v_lshl_add_u32 v17, v17, 6, v11
	v_mad_u32_u24 v17, v17, v21, v16
	v_lshl_add_u32 v18, v13, 7, v11
	v_subrev_u32_e32 v19, s66, v14
	v_mad_u32_u24 v18, v18, v21, v19
	v_cndmask_b32_e64 v26, v17, v18, s[56:57]
	v_mov_b32_e32 v22, s16
	v_mov_b32_e32 v23, s17
	v_mov_b32_e32 v24, s18
	v_mov_b32_e32 v25, s19
	v_cndmask_b32_e64 v22, v22, v24, s[58:59]
	v_cndmask_b32_e64 v23, v23, v25, s[58:59]
	v_mov_b32_e32 v24, s20
	v_mov_b32_e32 v25, s21
	v_cndmask_b32_e64 v22, v22, v24, s[56:57]
	v_cndmask_b32_e64 v23, v23, v25, s[56:57]
	v_mov_b32_e32 v27, 0
	v_lshl_add_u64 v[22:23], v[26:27], 2, v[22:23]
	s_or_b64 s[62:63], s[62:63], s[56:57]
	s_and_b64 exec, exec, s[62:63]
	global_load_dword v34, v[22:23], off
	s_mov_b64 exec, s[48:49]
	v_add_u32_e32 v10, s12, v10
	v_cmp_gt_u32_e32 vcc, s23, v10
	s_and_b64 exec, exec, vcc
	s_mov_b64 s[50:51], exec
	v_and_b32_e32 v11, 0x7f, v10
	v_lshrrev_b32_e32 v12, 7, v10
	v_lshrrev_b32_e32 v13, 7, v12
	v_mul_hi_u32 v13, v13, s22
	v_lshrrev_b32_e32 v13, 3, v13
	v_mul_u32_u24_e32 v14, 0x780, v13
	v_sub_u32_e32 v14, v12, v14
	v_cmp_le_u32_e64 s[56:57], s66, v14
	v_cmp_le_u32_e64 s[58:59], s67, v14
	v_mov_b32_e32 v35, 0
	v_cmp_gt_u32_e64 s[62:63], 64, v11
	v_cndmask_b32_e64 v15, 0, v20, s[58:59]
	v_sub_u32_e32 v15, v14, v15
	v_cmp_le_u32_e64 s[60:61], s68, v15
	s_nop 1
	v_cndmask_b32_e64 v16, 0, v21, s[60:61]
	v_sub_u32_e32 v16, v15, v16
	v_cndmask_b32_e64 v17, 0, 1, s[60:61]
	v_lshl_add_u32 v17, v13, 1, v17
	v_lshl_add_u32 v17, v17, 6, v11
	v_mad_u32_u24 v17, v17, v21, v16
	v_lshl_add_u32 v18, v13, 7, v11
	v_subrev_u32_e32 v19, s66, v14
	v_mad_u32_u24 v18, v18, v21, v19
	v_cndmask_b32_e64 v26, v17, v18, s[56:57]
	v_mov_b32_e32 v22, s16
	v_mov_b32_e32 v23, s17
	v_mov_b32_e32 v24, s18
	v_mov_b32_e32 v25, s19
	v_cndmask_b32_e64 v22, v22, v24, s[58:59]
	v_cndmask_b32_e64 v23, v23, v25, s[58:59]
	v_mov_b32_e32 v24, s20
	v_mov_b32_e32 v25, s21
	v_cndmask_b32_e64 v22, v22, v24, s[56:57]
	v_cndmask_b32_e64 v23, v23, v25, s[56:57]
	v_mov_b32_e32 v27, 0
	v_lshl_add_u64 v[22:23], v[26:27], 2, v[22:23]
	s_or_b64 s[62:63], s[62:63], s[56:57]
	s_and_b64 exec, exec, s[62:63]
	global_load_dword v35, v[22:23], off
	s_mov_b64 exec, s[50:51]
	v_add_u32_e32 v10, s12, v10
	v_cmp_gt_u32_e32 vcc, s23, v10
	s_and_b64 exec, exec, vcc
	s_mov_b64 s[52:53], exec
	v_and_b32_e32 v11, 0x7f, v10
	v_lshrrev_b32_e32 v12, 7, v10
	v_lshrrev_b32_e32 v13, 7, v12
	v_mul_hi_u32 v13, v13, s22
	v_lshrrev_b32_e32 v13, 3, v13
	v_mul_u32_u24_e32 v14, 0x780, v13
	v_sub_u32_e32 v14, v12, v14
	v_cmp_le_u32_e64 s[56:57], s66, v14
	v_cmp_le_u32_e64 s[58:59], s67, v14
	v_mov_b32_e32 v36, 0
	v_cmp_gt_u32_e64 s[62:63], 64, v11
	v_cndmask_b32_e64 v15, 0, v20, s[58:59]
	v_sub_u32_e32 v15, v14, v15
	v_cmp_le_u32_e64 s[60:61], s68, v15
	s_nop 1
	v_cndmask_b32_e64 v16, 0, v21, s[60:61]
	v_sub_u32_e32 v16, v15, v16
	v_cndmask_b32_e64 v17, 0, 1, s[60:61]
	v_lshl_add_u32 v17, v13, 1, v17
	v_lshl_add_u32 v17, v17, 6, v11
	v_mad_u32_u24 v17, v17, v21, v16
	v_lshl_add_u32 v18, v13, 7, v11
	v_subrev_u32_e32 v19, s66, v14
	v_mad_u32_u24 v18, v18, v21, v19
	v_cndmask_b32_e64 v26, v17, v18, s[56:57]
	v_mov_b32_e32 v22, s16
	v_mov_b32_e32 v23, s17
	v_mov_b32_e32 v24, s18
	v_mov_b32_e32 v25, s19
	v_cndmask_b32_e64 v22, v22, v24, s[58:59]
	v_cndmask_b32_e64 v23, v23, v25, s[58:59]
	v_mov_b32_e32 v24, s20
	v_mov_b32_e32 v25, s21
	v_cndmask_b32_e64 v22, v22, v24, s[56:57]
	v_cndmask_b32_e64 v23, v23, v25, s[56:57]
	v_mov_b32_e32 v27, 0
	v_lshl_add_u64 v[22:23], v[26:27], 2, v[22:23]
	s_or_b64 s[62:63], s[62:63], s[56:57]
	s_and_b64 exec, exec, s[62:63]
	global_load_dword v36, v[22:23], off
	s_mov_b64 exec, s[52:53]
	v_add_u32_e32 v10, s12, v10
	v_cmp_gt_u32_e32 vcc, s23, v10
	s_and_b64 exec, exec, vcc
	s_mov_b64 s[54:55], exec
	v_and_b32_e32 v11, 0x7f, v10
	v_lshrrev_b32_e32 v12, 7, v10
	v_lshrrev_b32_e32 v13, 7, v12
	v_mul_hi_u32 v13, v13, s22
	v_lshrrev_b32_e32 v13, 3, v13
	v_mul_u32_u24_e32 v14, 0x780, v13
	v_sub_u32_e32 v14, v12, v14
	v_cmp_le_u32_e64 s[56:57], s66, v14
	v_cmp_le_u32_e64 s[58:59], s67, v14
	v_mov_b32_e32 v37, 0
	v_cmp_gt_u32_e64 s[62:63], 64, v11
	v_cndmask_b32_e64 v15, 0, v20, s[58:59]
	v_sub_u32_e32 v15, v14, v15
	v_cmp_le_u32_e64 s[60:61], s68, v15
	s_nop 1
	v_cndmask_b32_e64 v16, 0, v21, s[60:61]
	v_sub_u32_e32 v16, v15, v16
	v_cndmask_b32_e64 v17, 0, 1, s[60:61]
	v_lshl_add_u32 v17, v13, 1, v17
	v_lshl_add_u32 v17, v17, 6, v11
	v_mad_u32_u24 v17, v17, v21, v16
	v_lshl_add_u32 v18, v13, 7, v11
	v_subrev_u32_e32 v19, s66, v14
	v_mad_u32_u24 v18, v18, v21, v19
	v_cndmask_b32_e64 v26, v17, v18, s[56:57]
	v_mov_b32_e32 v22, s16
	v_mov_b32_e32 v23, s17
	v_mov_b32_e32 v24, s18
	v_mov_b32_e32 v25, s19
	v_cndmask_b32_e64 v22, v22, v24, s[58:59]
	v_cndmask_b32_e64 v23, v23, v25, s[58:59]
	v_mov_b32_e32 v24, s20
	v_mov_b32_e32 v25, s21
	v_cndmask_b32_e64 v22, v22, v24, s[56:57]
	v_cndmask_b32_e64 v23, v23, v25, s[56:57]
	v_mov_b32_e32 v27, 0
	v_lshl_add_u64 v[22:23], v[26:27], 2, v[22:23]
	s_or_b64 s[62:63], s[62:63], s[56:57]
	s_and_b64 exec, exec, s[62:63]
	global_load_dword v37, v[22:23], off
	s_mov_b64 exec, s[54:55]
	v_add_u32_e32 v10, s12, v10
	v_cmp_gt_u32_e32 vcc, s23, v10
	s_and_b64 s[64:65], exec, vcc
	s_waitcnt vmcnt(0)
	s_mov_b64 exec, s[40:41]
	v_cvt_pk_bf16_f32 v30, v30, s0
	global_store_short v[4:5], v30, off
	v_lshl_add_u64 v[4:5], v[4:5], 0, s[14:15]
	s_mov_b64 exec, s[42:43]
	v_cvt_pk_bf16_f32 v31, v31, s0
	global_store_short v[4:5], v31, off
	v_lshl_add_u64 v[4:5], v[4:5], 0, s[14:15]
	s_mov_b64 exec, s[44:45]
	v_cvt_pk_bf16_f32 v32, v32, s0
	global_store_short v[4:5], v32, off
	v_lshl_add_u64 v[4:5], v[4:5], 0, s[14:15]
	s_mov_b64 exec, s[46:47]
	v_cvt_pk_bf16_f32 v33, v33, s0
	global_store_short v[4:5], v33, off
	v_lshl_add_u64 v[4:5], v[4:5], 0, s[14:15]
	s_mov_b64 exec, s[48:49]
	v_cvt_pk_bf16_f32 v34, v34, s0
	global_store_short v[4:5], v34, off
	v_lshl_add_u64 v[4:5], v[4:5], 0, s[14:15]
	s_mov_b64 exec, s[50:51]
	v_cvt_pk_bf16_f32 v35, v35, s0
	global_store_short v[4:5], v35, off
	v_lshl_add_u64 v[4:5], v[4:5], 0, s[14:15]
	s_mov_b64 exec, s[52:53]
	v_cvt_pk_bf16_f32 v36, v36, s0
	global_store_short v[4:5], v36, off
	v_lshl_add_u64 v[4:5], v[4:5], 0, s[14:15]
	s_mov_b64 exec, s[54:55]
	v_cvt_pk_bf16_f32 v37, v37, s0
	global_store_short v[4:5], v37, off
	v_lshl_add_u64 v[4:5], v[4:5], 0, s[14:15]
	s_mov_b64 exec, s[64:65]
	s_cbranch_execnz .Llora_trip

.LBB0_68:
	s_or_b64 exec, exec, s[10:11]
	s_mov_b64 s[10:11], 0x1000000
	v_cmp_gt_u64_e32 vcc, s[10:11], v[0:1]
	s_and_saveexec_b64 s[10:11], vcc
	s_cbranch_execz .LBB0_71
	s_ashr_i32 s3, s2, 31
	s_load_dwordx2 s[12:13], s[8:9], 0x0
	s_lshl_b64 s[8:9], s[2:3], 11
	s_lshl_b64 s[14:15], s[6:7], 12
	s_add_u32 s4, s4, s14
	s_addc_u32 s5, s5, s15
	v_lshl_add_u64 v[2:3], v[6:7], 3, s[4:5]
	s_mov_b64 s[4:5], 0x4100000
	v_lshl_add_u64 v[2:3], v[2:3], 0, s[4:5]
	s_lshl_b64 s[4:5], s[2:3], 12
	s_lshl_b64 s[6:7], s[6:7], 13
	s_waitcnt lgkmcnt(0)
	s_add_u32 s6, s12, s6
	s_addc_u32 s7, s13, s7
	v_lshl_add_u64 v[4:5], v[6:7], 4, s[6:7]
	s_lshl_b64 s[2:3], s[2:3], 13
	s_mov_b64 s[6:7], 0
	s_mov_b64 s[12:13], 0x1000000
.LBB0_70:
	s_mov_b64 s[14:15], exec
	global_load_dwordx4 v[30:33], v[4:5], off
	v_lshl_add_u64 v[0:1], v[0:1], 0, s[8:9]
	v_lshl_add_u64 v[4:5], v[4:5], 0, s[2:3]
	v_cmp_gt_u64_e32 vcc, s[12:13], v[0:1]
	s_and_b64 exec, exec, vcc
	s_mov_b64 s[16:17], exec
	global_load_dwordx4 v[34:37], v[4:5], off
	v_lshl_add_u64 v[0:1], v[0:1], 0, s[8:9]
	v_lshl_add_u64 v[4:5], v[4:5], 0, s[2:3]
	v_cmp_gt_u64_e32 vcc, s[12:13], v[0:1]
	s_and_b64 exec, exec, vcc
	s_mov_b64 s[18:19], exec
	global_load_dwordx4 v[38:41], v[4:5], off
	v_lshl_add_u64 v[0:1], v[0:1], 0, s[8:9]
	v_lshl_add_u64 v[4:5], v[4:5], 0, s[2:3]
	v_cmp_gt_u64_e32 vcc, s[12:13], v[0:1]
	s_and_b64 exec, exec, vcc
	s_mov_b64 s[20:21], exec
	global_load_dwordx4 v[42:45], v[4:5], off
	v_lshl_add_u64 v[0:1], v[0:1], 0, s[8:9]
	v_lshl_add_u64 v[4:5], v[4:5], 0, s[2:3]
	v_cmp_gt_u64_e32 vcc, s[12:13], v[0:1]
	s_and_b64 exec, exec, vcc
	s_mov_b64 s[22:23], exec
	global_load_dwordx4 v[46:49], v[4:5], off
	v_lshl_add_u64 v[0:1], v[0:1], 0, s[8:9]
	v_lshl_add_u64 v[4:5], v[4:5], 0, s[2:3]
	v_cmp_gt_u64_e32 vcc, s[12:13], v[0:1]
	s_and_b64 exec, exec, vcc
	s_mov_b64 s[24:25], exec
	global_load_dwordx4 v[50:53], v[4:5], off
	v_lshl_add_u64 v[0:1], v[0:1], 0, s[8:9]
	v_lshl_add_u64 v[4:5], v[4:5], 0, s[2:3]
	v_cmp_gt_u64_e32 vcc, s[12:13], v[0:1]
	s_and_b64 exec, exec, vcc
	s_mov_b64 s[26:27], exec
	global_load_dwordx4 v[54:57], v[4:5], off
	v_lshl_add_u64 v[0:1], v[0:1], 0, s[8:9]
	v_lshl_add_u64 v[4:5], v[4:5], 0, s[2:3]
	v_cmp_gt_u64_e32 vcc, s[12:13], v[0:1]
	s_and_b64 exec, exec, vcc
	s_mov_b64 s[28:29], exec
	global_load_dwordx4 v[58:61], v[4:5], off
	v_lshl_add_u64 v[0:1], v[0:1], 0, s[8:9]
	v_lshl_add_u64 v[4:5], v[4:5], 0, s[2:3]
	v_cmp_gt_u64_e32 vcc, s[12:13], v[0:1]
	s_and_b64 s[34:35], exec, vcc
	s_mov_b64 exec, s[14:15]
	s_waitcnt vmcnt(0)
	v_cvt_pk_bf16_f32 v30, v30, v31
	v_cvt_pk_bf16_f32 v31, v32, v33
	global_store_dwordx2 v[2:3], v[30:31], off
	v_lshl_add_u64 v[2:3], v[2:3], 0, s[4:5]
	s_mov_b64 exec, s[16:17]
	v_cvt_pk_bf16_f32 v34, v34, v35
	v_cvt_pk_bf16_f32 v35, v36, v37
	global_store_dwordx2 v[2:3], v[34:35], off
	v_lshl_add_u64 v[2:3], v[2:3], 0, s[4:5]
	s_mov_b64 exec, s[18:19]
	v_cvt_pk_bf16_f32 v38, v38, v39
	v_cvt_pk_bf16_f32 v39, v40, v41
	global_store_dwordx2 v[2:3], v[38:39], off
	v_lshl_add_u64 v[2:3], v[2:3], 0, s[4:5]
	s_mov_b64 exec, s[20:21]
	v_cvt_pk_bf16_f32 v42, v42, v43
	v_cvt_pk_bf16_f32 v43, v44, v45
	global_store_dwordx2 v[2:3], v[42:43], off
	v_lshl_add_u64 v[2:3], v[2:3], 0, s[4:5]
	s_mov_b64 exec, s[22:23]
	v_cvt_pk_bf16_f32 v46, v46, v47
	v_cvt_pk_bf16_f32 v47, v48, v49
	global_store_dwordx2 v[2:3], v[46:47], off
	v_lshl_add_u64 v[2:3], v[2:3], 0, s[4:5]
	s_mov_b64 exec, s[24:25]
	v_cvt_pk_bf16_f32 v50, v50, v51
	v_cvt_pk_bf16_f32 v51, v52, v53
	global_store_dwordx2 v[2:3], v[50:51], off
	v_lshl_add_u64 v[2:3], v[2:3], 0, s[4:5]
	s_mov_b64 exec, s[26:27]
	v_cvt_pk_bf16_f32 v54, v54, v55
	v_cvt_pk_bf16_f32 v55, v56, v57
	global_store_dwordx2 v[2:3], v[54:55], off
	v_lshl_add_u64 v[2:3], v[2:3], 0, s[4:5]
	s_mov_b64 exec, s[28:29]
	v_cvt_pk_bf16_f32 v58, v58, v59
	v_cvt_pk_bf16_f32 v59, v60, v61
	global_store_dwordx2 v[2:3], v[58:59], off
	v_lshl_add_u64 v[2:3], v[2:3], 0, s[4:5]
	s_mov_b64 exec, s[34:35]
	s_cbranch_execnz .LBB0_70
